# baseline (speedup 1.0000x reference)
.LBB0_37:
	s_or_b64 exec, exec, s[0:1]
	v_mov_b32_e32 v98, v97
	v_mov_b32_e32 v99, v97
	v_mov_b32_e32 v5, v97
	v_mov_b32_e32 v6, v97
	v_mov_b32_e32 v7, v97
	v_mov_b32_e32 v1, v97
	v_mov_b32_e32 v2, v97
	v_mov_b32_e32 v3, v97
	s_mov_b32 s0, 0x10000
	v_or_b32_e32 v8, 0x21000, v223
	v_mfma_f32_32x32x16_f16 v[32:47], v[96:99], v[0:3], 0
	v_mfma_f32_32x32x16_f16 v[16:31], v[4:7], v[0:3], 0
	v_or_b32_e32 v114, 0x21000, v223
	v_cmp_eq_u32_e64 s[0:1], 0, v225
	s_and_b64 vcc, vcc, s[0:1]
	ds_read_b128 v[8:11], v114
	ds_read_b128 v[12:15], v114 offset:32
	ds_read_b128 v[234:237], v114 offset:64
	ds_read_b128 v[238:241], v114 offset:96
	ds_read_b128 v[242:245], v114 offset:128
	ds_read_b128 v[106:109], v114 offset:160
	ds_read_b128 v[110:113], v114 offset:192
	s_waitcnt lgkmcnt(7)
	v_mfma_f32_32x32x16_f16 v[32:47], v[180:183], v[92:95], v[32:47]
	ds_read_b128 v[0:3], v114 offset:224
	v_mfma_f32_32x32x16_f16 v[32:47], v[184:187], v[88:91], v[32:47]
	v_mfma_f32_32x32x16_f16 v[32:47], v[188:191], v[84:87], v[32:47]
	v_mfma_f32_32x32x16_f16 v[32:47], v[192:195], v[80:83], v[32:47]
	v_mfma_f32_32x32x16_f16 v[32:47], v[196:199], v[76:79], v[32:47]
	v_mfma_f32_32x32x16_f16 v[32:47], v[200:203], v[72:75], v[32:47]
	v_mfma_f32_32x32x16_f16 v[32:47], v[204:207], v[68:71], v[32:47]
	v_mfma_f32_32x32x16_f16 v[32:47], v[208:211], v[64:67], v[32:47]
	s_waitcnt lgkmcnt(0)
	s_cmp_lg_u64 s[4:5], 0
	s_cbranch_scc1 .Lt1_full
	v_mfma_f32_32x32x16_f16 v[16:31], v[148:151], v[92:95], v[16:31]
	v_mfma_f32_32x32x16_f16 v[16:31], v[152:155], v[88:91], v[16:31]
	v_mfma_f32_32x32x16_f16 v[16:31], v[156:159], v[84:87], v[16:31]
	v_mfma_f32_32x32x16_f16 v[16:31], v[160:163], v[80:83], v[16:31]
	v_mfma_f32_32x32x16_f16 v[16:31], v[164:167], v[76:79], v[16:31]
	v_mfma_f32_32x32x16_f16 v[16:31], v[168:171], v[72:75], v[16:31]
	v_mfma_f32_32x32x16_f16 v[16:31], v[172:175], v[68:71], v[16:31]
	s_nop 3
	s_branch .Lt1_ks7
.Lt1_full:
	v_dot2c_f32_f16_e32 v98, v92, v8
	v_mfma_f32_32x32x16_f16 v[16:31], v[148:151], v[92:95], v[16:31]
	v_dot2c_f32_f16_e32 v98, v93, v9
	v_dot2c_f32_f16_e32 v98, v94, v10
	v_dot2c_f32_f16_e32 v98, v95, v11
	v_dot2c_f32_f16_e32 v98, v88, v12
	v_mfma_f32_32x32x16_f16 v[16:31], v[152:155], v[88:91], v[16:31]
	v_dot2c_f32_f16_e32 v98, v89, v13
	v_dot2c_f32_f16_e32 v98, v90, v14
	v_dot2c_f32_f16_e32 v98, v91, v15
	v_dot2c_f32_f16_e32 v98, v84, v234
	v_mfma_f32_32x32x16_f16 v[16:31], v[156:159], v[84:87], v[16:31]
	v_dot2c_f32_f16_e32 v98, v85, v235
	v_dot2c_f32_f16_e32 v98, v86, v236
	v_dot2c_f32_f16_e32 v98, v87, v237
	v_dot2c_f32_f16_e32 v98, v80, v238
	v_mfma_f32_32x32x16_f16 v[16:31], v[160:163], v[80:83], v[16:31]
	v_dot2c_f32_f16_e32 v98, v81, v239
	v_dot2c_f32_f16_e32 v98, v82, v240
	v_dot2c_f32_f16_e32 v98, v83, v241
	v_dot2c_f32_f16_e32 v98, v76, v242
	v_mfma_f32_32x32x16_f16 v[16:31], v[164:167], v[76:79], v[16:31]
	v_dot2c_f32_f16_e32 v98, v77, v243
	v_dot2c_f32_f16_e32 v98, v78, v244
	v_dot2c_f32_f16_e32 v98, v79, v245
	v_dot2c_f32_f16_e32 v98, v72, v106
	v_mfma_f32_32x32x16_f16 v[16:31], v[168:171], v[72:75], v[16:31]
	v_dot2c_f32_f16_e32 v98, v73, v107
	v_dot2c_f32_f16_e32 v98, v74, v108
	v_dot2c_f32_f16_e32 v98, v75, v109
	v_dot2c_f32_f16_e32 v98, v68, v110
	v_mfma_f32_32x32x16_f16 v[16:31], v[172:175], v[68:71], v[16:31]
	v_dot2c_f32_f16_e32 v98, v69, v111
	v_dot2c_f32_f16_e32 v98, v70, v112
	v_dot2c_f32_f16_e32 v98, v71, v113
.Lt1_ks7:
	v_cvt_pk_f16_f32 v7, v38, v39
	v_cvt_pk_f16_f32 v6, v36, v37
	v_cvt_pk_f16_f32 v5, v34, v35
	v_cvt_pk_f16_f32 v4, v32, v33
	v_dot2c_f32_f16_e32 v98, v64, v0
	v_dot2c_f32_f16_e32 v98, v65, v1
	v_dot2c_f32_f16_e32 v98, v66, v2
	v_mfma_f32_32x32x16_f16 v[16:31], v[176:179], v[64:67], v[16:31]
	v_dot2c_f32_f16_e32 v98, v67, v3
	v_cvt_pk_f16_f32 v35, v46, v47
	v_cvt_pk_f16_f32 v34, v44, v45
	v_cvt_pk_f16_f32 v33, v42, v43
	v_cvt_pk_f16_f32 v32, v40, v41
	ds_bpermute_b32 v36, v102, v98
	v_cvt_f32_i32_e32 v37, v226
	v_mfma_f32_32x32x16_f16 v[0:15], v[4:7], v[60:63], 0
	s_nop 3
	v_cvt_pk_f16_f32 v23, v22, v23
	v_cvt_pk_f16_f32 v22, v20, v21
	v_cvt_pk_f16_f32 v21, v18, v19
	v_cvt_pk_f16_f32 v20, v16, v17
	v_cvt_pk_f16_f32 v19, v30, v31
	v_cvt_pk_f16_f32 v18, v28, v29
	v_cvt_pk_f16_f32 v17, v26, v27
	v_mfma_f32_32x32x16_f16 v[0:15], v[32:35], v[56:59], v[0:15]
	v_cvt_pk_f16_f32 v16, v24, v25
	s_waitcnt lgkmcnt(0)
	v_add_f32_e32 v36, v98, v36
	v_cvt_f16_f32_e32 v26, v100
	v_mov_b32_e32 v98, v97
	v_lshlrev_b32_e32 v32, 4, v218
	v_mfma_f32_32x32x16_f16 v[0:15], v[20:23], v[52:55], v[0:15]
	v_fma_mixlo_f16 v20, v37, v104, v36
	v_pack_b32_f16 v20, v20, 0
	v_pack_b32_f16 v21, v26, 0
	v_cndmask_b32_e32 v96, 0, v21, vcc
	v_mfma_f32_32x32x16_f16 v[0:15], v[16:19], v[48:51], v[0:15]
	v_cndmask_b32_e32 v16, 0, v20, vcc
	v_mov_b32_e32 v17, v97
	v_mov_b32_e32 v18, v97
	v_mov_b32_e32 v19, v97
	v_cmp_ne_u32_e32 vcc, 0, v225
	s_nop 0
	v_mfma_f32_32x32x16_f16 v[0:15], v[16:19], v[96:99], v[0:15]
	v_lshlrev_b32_e32 v70, 2, v215
	v_lshl_add_u32 v70, v214, 4, v70
	global_load_dwordx4 v[16:19], v70, s[64:65]
	global_load_dwordx4 v[20:23], v70, s[64:65] offset:32
	global_load_dwordx4 v[24:27], v70, s[64:65] offset:64
	global_load_dwordx4 v[28:31], v70, s[64:65] offset:96
	s_and_saveexec_b64 s[6:7], vcc
	s_cbranch_execz .LBB0_39
	v_lshl_or_b32 v71, v251, 12, v32
	v_add_u32_e32 v71, 0x18800, v71
	s_nop 7
	ds_write_b128 v71, v[0:3]
	ds_write_b128 v71, v[4:7] offset:1024
	ds_write_b128 v71, v[8:11] offset:2048
	ds_write_b128 v71, v[12:15] offset:3072
